# DA: tile j+2 LDS-DMA issue moved behind the QK MFMAs (on 4-bit K swizzle) m1
# speedup vs baseline: 1.0103x; 1.0027x over previous
; __device__ __forceinline__ void da_unit(LAS unsigned char* lds, const bf16* __restrict__ Q, const bf16* __restrict__ Kp, const bf16* __restrict__ Vp, const float* __restrict__ gda, float lam, ...
;     ...
;         const int buf = kbuf;
;         if (j + 1 < NT) asm volatile("s_waitcnt vmcnt(4)" ::: "memory"); else asm volatile("s_waitcnt vmcnt(0)" ::: "memory");
;         __syncthreads();
;         if (j + 2 < NT) att_dma(dm, Kh, Vh, (j + 2) * 64, K_lds + (kbuf == 0 ? 2 : kbuf - 1) * SHM_T, V_lds + ((vbuf + 2) & 3) * SHM_T, wave);
;         if (comp == 1 && pend) { pv_pipe(o, vb0 + pbuf * SHM_T, pa0, pa1, pa2, pa3); pend = false; }
.LBB0_579:
	s_add_i32 s8, s27, 5
	s_cmp_ge_u32 s8, s24
	s_barrier
	s_cbranch_scc1 .LBB0_582
	s_and_b64 s[8:9], s[12:13], s[18:19]
	s_andn2_b64 vcc, exec, s[8:9]
	s_cbranch_vccz .LBB0_583

; #define LAS __attribute__((address_space(3)))
; #define SBAR() __builtin_amdgcn_sched_barrier(0)
; __device__ __forceinline__ void da_unit(LAS unsigned char* lds, const bf16* __restrict__ Q, const bf16* __restrict__ Kp, const bf16* __restrict__ Vp, const float* __restrict__ gda, float lam, ...
;     ...
;         if (j + 2 < NT) att_dma(dm, Kh, Vh, (j + 2) * 64, K_lds + (kbuf == 0 ? 2 : kbuf - 1) * SHM_T, V_lds + ((vbuf + 2) & 3) * SHM_T, wave);
;         if (comp == 1 && pend) { pv_pipe(o, vb0 + pbuf * SHM_T, pa0, pa1, pa2, pa3); pend = false; }
;         if (j < NTw) {
;             f32x16 p0 = mneg, p1 = mneg;
;             { const LAS unsigned char* Ks = K_lds + buf * SHM_T; bf16x8 kb0[4], kb1[4];
; #pragma unroll
;               for (int d0 = 0; d0 < 4; ++d0) { const int cb = (comp * 64 + d0 * 16 + hi * 8) * 2;
;                   kb0[d0] = *(const LAS bf16x8*)(Ks + KSWZ(r32, cb)); kb1[d0] = *(const LAS bf16x8*)(Ks + KSWZ(32 + r32, cb)); }
;               SBAR();
; #pragma unroll
;               for (int d0 = 0; d0 < 4; ++d0) { p0 = __builtin_amdgcn_mfma_f32_32x32x16_bf16(kb0[d0], qr[d0], p0, 0, 0, 0); p1 = __builtin_amdgcn_mfma_f32_32x32x16_bf16(kb1[d0], qr[d0], p1, 0, 0, 0); } }
;             if (j == 0) {
; #pragma unroll
;                 for (int r = 0; r < 16; ++r) p0[r] = -INFINITY;
; #pragma unroll
;                 for (int r = 0; r < 8; ++r) p1[r] = -INFINITY;
;             }
;             float pmax = p0[0];
; #pragma unroll
;             for (int r = 1; r < 16; ++r) pmax = fmaxf(pmax, p0[r]);
; #pragma unroll
;             for (int r = 0; r < 16; ++r) pmax = fmaxf(pmax, p1[r]);
;             { auto rr = __builtin_amdgcn_permlane32_swap(__builtin_bit_cast(unsigned, pmax), __builtin_bit_cast(unsigned, pmax), false, false);
;               pmax = fmaxf(__builtin_bit_cast(float, rr[0]), __builtin_bit_cast(float, rr[1])); }
;             float alpha = 1.f;
;             if (j == 0 || !__all(pmax <= THR2)) {
;                 const float dl = j == 0 ? pmax : fmaxf(pmax, 0.f);
;                 alpha = j == 0 ? 1.f : __builtin_amdgcn_exp2f(-dl); m_reg += dl;
; #pragma unroll
;                 for (int r = 0; r < 16; ++r) { p0[r] -= dl; p1[r] -= dl; mneg[r] = -m_reg; }
.LBB0_584:
	s_lshl_b32 s8, s23, 14
	s_add_i32 s8, s8, 0
	s_add_i32 s8, s8, 0x10000
	v_add_u32_e32 v82, s8, v165
	v_add_u32_e32 v83, s8, v170
	v_add_u32_e32 v84, v82, v173
	v_add_u32_e32 v85, v83, v173
	ds_read_b128 v[98:101], v84
	ds_read_b128 v[182:185], v85
	v_add_u32_e32 v84, v82, v174
	v_add_u32_e32 v85, v83, v174
	ds_read_b128 v[186:189], v84
	ds_read_b128 v[190:193], v85
	v_add_u32_e32 v84, v82, v175
	v_add_u32_e32 v82, v82, v176
	v_add_u32_e32 v85, v83, v175
	ds_read_b128 v[196:199], v84
	ds_read_b128 v[200:203], v85
	v_add_u32_e32 v83, v83, v176
	ds_read_b128 v[204:207], v82
	ds_read_b128 v[208:211], v83
	s_waitcnt lgkmcnt(7)
	s_setprio 1
	v_mfma_f32_32x32x16_bf16 v[82:97], v[98:101], v[114:117], v[66:81]
	v_mov_b64_e32 v[112:113], v[80:81]
	v_mov_b64_e32 v[110:111], v[78:79]
	v_mov_b64_e32 v[108:109], v[76:77]
	v_mov_b64_e32 v[106:107], v[74:75]
	v_mov_b64_e32 v[104:105], v[72:73]
	v_mov_b64_e32 v[102:103], v[70:71]
	v_mov_b64_e32 v[100:101], v[68:69]
	v_mov_b64_e32 v[98:99], v[66:67]
	s_waitcnt lgkmcnt(5)
	v_mfma_f32_32x32x16_bf16 v[82:97], v[186:189], v[118:121], v[82:97]
	s_mov_b32 s8, 0x4138aa3b
	v_mfma_f32_32x32x16_bf16 v[98:113], v[182:185], v[114:117], v[98:113]
	s_waitcnt lgkmcnt(3)
	v_mfma_f32_32x32x16_bf16 v[82:97], v[196:199], v[122:125], v[82:97]
	v_mfma_f32_32x32x16_bf16 v[98:113], v[190:193], v[118:121], v[98:113]
	s_waitcnt lgkmcnt(1)
	v_mfma_f32_32x32x16_bf16 v[82:97], v[204:207], v[126:129], v[82:97]
	v_mfma_f32_32x32x16_bf16 v[98:113], v[200:203], v[122:125], v[98:113]
	s_add_i32 s98, s27, 5
	s_cmp_ge_u32 s98, s24
	s_cbranch_scc1 .Lda_nodma
	s_lshl_b32 s98, s23, 14
	s_addk_i32 s98, 0xc000
	s_cmp_lg_u32 s23, 0
	s_cselect_b32 s98, s98, 0x8000
	s_lshl_b32 s99, s29, 14
	s_xor_b32 s99, s99, 0x8000
	s_add_i32 s98, s76, s98
	s_mov_b32 m0, s98
	s_add_i32 s99, s57, s99
	buffer_load_dwordx4 v247, s[4:7], s28 offen lds
	s_mov_b32 s66, s6
	s_mov_b32 s67, s7
	s_mov_b32 m0, s99
	s_nop 0
	buffer_load_dwordx4 v137, s[64:67], s28 offen lds
	s_add_i32 m0, s98, 0x2000
	s_nop 0
	buffer_load_dwordx4 v248, s[4:7], s28 offen lds
	s_add_i32 m0, s99, 0x2000
	s_nop 0
	buffer_load_dwordx4 v141, s[64:67], s28 offen lds
	s_branch .Lda_dmadone
.Lda_nodma:
	s_nop 10
.Lda_dmadone:
	v_max_f32_e32 v182, v83, v83
	v_max_f32_e32 v183, v82, v82
	v_max_f32_e32 v182, v183, v182
	v_max3_f32 v182, v182, v84, v85
	v_max3_f32 v182, v182, v86, v87
	v_max3_f32 v182, v182, v88, v89
	v_max3_f32 v182, v182, v90, v91
	s_waitcnt lgkmcnt(0)
	v_mfma_f32_32x32x16_bf16 v[98:113], v[208:211], v[126:129], v[98:113]
	s_setprio 0
	v_max3_f32 v182, v182, v92, v93
	v_max3_f32 v182, v182, v94, v95
	v_max3_f32 v182, v182, v96, v97
	s_nop 8
	v_max3_f32 v182, v182, v98, v99
	v_max3_f32 v182, v182, v100, v101
	v_max3_f32 v182, v182, v102, v103
	v_max3_f32 v182, v182, v104, v105
	v_max3_f32 v182, v182, v106, v107
	v_max3_f32 v182, v182, v108, v109
	v_max3_f32 v182, v182, v110, v111
	v_max3_f32 v183, v182, v112, v113
	v_mov_b32_e32 v182, v183
	s_nop 1
	v_permlane32_swap_b32_e32 v183, v182
	v_cmp_ge_f32_e32 vcc, s8, v183
	s_cmp_eq_u64 vcc, exec
	v_mov_b32_e32 v182, 1.0
	s_cbranch_scc1 .LBB0_586
	v_max_f32_e32 v66, v183, v183
	v_max_f32_e32 v68, 0, v66
	v_exp_f32_e64 v182, -v68
	v_add_f32_e32 v151, v151, v68
	v_xor_b32_e32 v66, 0x80000000, v151
	v_pk_add_f32 v[82:83], v[82:83], v[68:69] op_sel_hi:[1,0] neg_lo:[0,1] neg_hi:[0,1]
	v_pk_add_f32 v[98:99], v[98:99], v[68:69] op_sel_hi:[1,0] neg_lo:[0,1] neg_hi:[0,1]
	v_pk_add_f32 v[84:85], v[84:85], v[68:69] op_sel_hi:[1,0] neg_lo:[0,1] neg_hi:[0,1]
	v_pk_add_f32 v[100:101], v[100:101], v[68:69] op_sel_hi:[1,0] neg_lo:[0,1] neg_hi:[0,1]
	v_pk_add_f32 v[86:87], v[86:87], v[68:69] op_sel_hi:[1,0] neg_lo:[0,1] neg_hi:[0,1]
	v_pk_add_f32 v[102:103], v[102:103], v[68:69] op_sel_hi:[1,0] neg_lo:[0,1] neg_hi:[0,1]
	v_pk_add_f32 v[88:89], v[88:89], v[68:69] op_sel_hi:[1,0] neg_lo:[0,1] neg_hi:[0,1]
	v_pk_add_f32 v[104:105], v[104:105], v[68:69] op_sel_hi:[1,0] neg_lo:[0,1] neg_hi:[0,1]
	v_pk_add_f32 v[90:91], v[90:91], v[68:69] op_sel_hi:[1,0] neg_lo:[0,1] neg_hi:[0,1]
	v_pk_add_f32 v[106:107], v[106:107], v[68:69] op_sel_hi:[1,0] neg_lo:[0,1] neg_hi:[0,1]
	v_pk_add_f32 v[92:93], v[92:93], v[68:69] op_sel_hi:[1,0] neg_lo:[0,1] neg_hi:[0,1]
	v_pk_add_f32 v[108:109], v[108:109], v[68:69] op_sel_hi:[1,0] neg_lo:[0,1] neg_hi:[0,1]
	v_pk_add_f32 v[94:95], v[94:95], v[68:69] op_sel_hi:[1,0] neg_lo:[0,1] neg_hi:[0,1]
	v_pk_add_f32 v[110:111], v[110:111], v[68:69] op_sel_hi:[1,0] neg_lo:[0,1] neg_hi:[0,1]
	v_pk_add_f32 v[96:97], v[96:97], v[68:69] op_sel_hi:[1,0] neg_lo:[0,1] neg_hi:[0,1]
	v_pk_add_f32 v[112:113], v[112:113], v[68:69] op_sel_hi:[1,0] neg_lo:[0,1] neg_hi:[0,1]
	v_mov_b32_e32 v67, v66
	v_mov_b32_e32 v68, v66
	v_mov_b32_e32 v69, v66
	v_mov_b32_e32 v70, v66
	v_mov_b32_e32 v71, v66
	v_mov_b32_e32 v72, v66
	v_mov_b32_e32 v73, v66
	v_mov_b32_e32 v74, v66
	v_mov_b32_e32 v75, v66
	v_mov_b32_e32 v76, v66
	v_mov_b32_e32 v77, v66
	v_mov_b32_e32 v78, v66
	v_mov_b32_e32 v79, v66
	v_mov_b32_e32 v80, v66
	v_mov_b32_e32 v81, v66

; __global__ void __launch_bounds__(NWAVES * 64, 2) fwd(Args args) {
	.amdhsa_kernel _Z3fwd4Args
		.amdhsa_group_segment_fixed_size 0
		.amdhsa_private_segment_fixed_size 0
		.amdhsa_kernarg_size 432
		.amdhsa_user_sgpr_count 2
		.amdhsa_user_sgpr_dispatch_ptr 0
		.amdhsa_user_sgpr_queue_ptr 0
		.amdhsa_user_sgpr_kernarg_segment_ptr 1
		.amdhsa_user_sgpr_dispatch_id 0
		.amdhsa_user_sgpr_kernarg_preload_length 0
		.amdhsa_user_sgpr_kernarg_preload_offset 0
		.amdhsa_user_sgpr_private_segment_size 0
		.amdhsa_uses_dynamic_stack 0
		.amdhsa_enable_private_segment 0
		.amdhsa_system_sgpr_workgroup_id_x 1
		.amdhsa_system_sgpr_workgroup_id_y 0
		.amdhsa_system_sgpr_workgroup_id_z 0
		.amdhsa_system_sgpr_workgroup_info 0
		.amdhsa_system_vgpr_workitem_id 0
		.amdhsa_next_free_vgpr 250
		.amdhsa_next_free_sgpr 102
		.amdhsa_accum_offset 252
		.amdhsa_reserve_vcc 1
		.amdhsa_float_round_mode_32 0
		.amdhsa_float_round_mode_16_64 0
		.amdhsa_float_denorm_mode_32 3
		.amdhsa_float_denorm_mode_16_64 3
		.amdhsa_dx10_clamp 1
		.amdhsa_ieee_mode 1
		.amdhsa_fp16_overflow 0
		.amdhsa_tg_split 0
		.amdhsa_exception_fp_ieee_invalid_op 0
		.amdhsa_exception_fp_denorm_src 0
		.amdhsa_exception_fp_ieee_div_zero 0
		.amdhsa_exception_fp_ieee_overflow 0
		.amdhsa_exception_fp_ieee_underflow 0
		.amdhsa_exception_fp_ieee_inexact 0
		.amdhsa_exception_int_div_zero 0
	.end_amdhsa_kernel

; __global__ void __launch_bounds__(NWAVES * 64, 2) fwd(Args args) {
amdhsa.kernels:
  - .agpr_count:     0
    .args:
      - .offset:         0
        .size:           176
        .value_kind:     by_value
      - .offset:         176
        .size:           4
        .value_kind:     hidden_block_count_x
      - .offset:         180
        .size:           4
        .value_kind:     hidden_block_count_y
      - .offset:         184
        .size:           4
        .value_kind:     hidden_block_count_z
      - .offset:         188
        .size:           2
        .value_kind:     hidden_group_size_x
      - .offset:         190
        .size:           2
        .value_kind:     hidden_group_size_y
      - .offset:         192
        .size:           2
        .value_kind:     hidden_group_size_z
      - .offset:         194
        .size:           2
        .value_kind:     hidden_remainder_x
      - .offset:         196
        .size:           2
        .value_kind:     hidden_remainder_y
      - .offset:         198
        .size:           2
        .value_kind:     hidden_remainder_z
      - .offset:         216
        .size:           8
        .value_kind:     hidden_global_offset_x
      - .offset:         224
        .size:           8
        .value_kind:     hidden_global_offset_y
      - .offset:         232
        .size:           8
        .value_kind:     hidden_global_offset_z
      - .offset:         240
        .size:           2
        .value_kind:     hidden_grid_dims
      - .offset:         296
        .size:           4
        .value_kind:     hidden_dynamic_lds_size
    .group_segment_fixed_size: 0
    .kernarg_segment_align: 8
    .kernarg_segment_size: 432
    .language:       OpenCL C
    .language_version:
      - 2
      - 0
    .max_flat_workgroup_size: 512
    .name:           _Z3fwd4Args
    .private_segment_fixed_size: 0
    .sgpr_count:     108
    .sgpr_spill_count: 40
    .symbol:         _Z3fwd4Args.kd
    .uniform_work_group_size: 1
    .uses_dynamic_stack: false
    .vgpr_count:     250
    .vgpr_spill_count: 0
    .wavefront_size: 64
